# flat-release barrier, invalidate moved after the arrival result: leader issues wbl2 then inv and waits only for the wbl2 (vmcnt(1)) before releasing; non-leaders invalidate after the arrival atomic re
# speedup vs baseline: 1.0040x; 1.0040x over previous
.LBB0_69:
	s_lshl_b32 s4, s33, 8
	s_add_u32 s4, s14, s4
	s_addc_u32 s5, s15, 0
	v_mov_b32_e32 v2, 0x1000
	v_mov_b32_e32 v4, 1
	global_atomic_add v4, v2, v4, s[4:5] offset:1024 sc0
	s_nop 0
	v_cvt_f32_u32_e32 v2, v3
	v_sub_u32_e32 v5, 0, v3
	v_rcp_iflag_f32_e32 v2, v2
	s_nop 0
	v_mul_f32_e32 v2, 0x4f7ffffe, v2
	v_cvt_u32_f32_e32 v2, v2
	v_mul_lo_u32 v5, v5, v2
	v_mul_hi_u32 v5, v2, v5
	v_add_u32_e32 v2, v2, v5
	s_waitcnt vmcnt(0)
	v_mul_hi_u32 v2, v4, v2
	v_mul_lo_u32 v5, v2, v3
	v_sub_u32_e32 v5, v4, v5
	v_add_u32_e32 v6, 1, v2
	v_cmp_ge_u32_e32 vcc, v5, v3
	v_add_u32_e32 v4, 1, v4
	s_nop 0
	v_cndmask_b32_e32 v2, v2, v6, vcc
	v_sub_u32_e32 v6, v5, v3
	v_cndmask_b32_e32 v5, v5, v6, vcc
	v_add_u32_e32 v6, 1, v2
	v_cmp_ge_u32_e32 vcc, v5, v3
	s_nop 1
	v_cndmask_b32_e32 v2, v2, v6, vcc
	v_mul_lo_u32 v5, v3, v2
	v_add_u32_e32 v3, v5, v3
	v_cmp_ne_u32_e32 vcc, v4, v3
	v_sub_u32_e32 v6, v3, v5
	s_waitcnt lgkmcnt(0)
	v_mov_b32_e32 v1, 0
	v_add_u32_e32 v2, 1, v2
	v_lshlrev_b32_e32 v2, 8, v2
	s_add_u32 s8, s4, 0x2400
	s_addc_u32 s9, s5, 0
	s_waitcnt lgkmcnt(0)
	s_cbranch_vccnz .Lnb_nl_99
	buffer_wbl2 sc1
	buffer_inv sc1
	s_add_u32 s12, s16, 0x6400
	s_addc_u32 s13, s17, 0
	s_mov_b32 s10, 16
	s_waitcnt vmcnt(1)

.Lnb_nl_99:
	buffer_inv sc1

.LBB0_170:
	v_readlane_b32 s4, v253, 8
	v_readlane_b32 s5, v253, 9
	v_cvt_f32_u32_e32 v1, v4
	v_sub_u32_e32 v6, 0, v4
	v_rcp_iflag_f32_e32 v1, v1
	s_nop 1
	global_atomic_add v5, v3, v228, s[4:5] sc0
	s_nop 0
	v_mul_f32_e32 v1, 0x4f7ffffe, v1
	v_cvt_u32_f32_e32 v1, v1
	v_mul_lo_u32 v6, v6, v1
	v_mul_hi_u32 v6, v1, v6
	v_add_u32_e32 v1, v1, v6
	s_waitcnt vmcnt(0)
	v_mul_hi_u32 v1, v5, v1
	v_mul_lo_u32 v6, v1, v4
	v_sub_u32_e32 v6, v5, v6
	v_add_u32_e32 v7, 1, v1
	v_cmp_ge_u32_e32 vcc, v6, v4
	v_add_u32_e32 v5, 1, v5
	s_nop 0
	v_cndmask_b32_e32 v1, v1, v7, vcc
	v_sub_u32_e32 v7, v6, v4
	v_cndmask_b32_e32 v6, v6, v7, vcc
	v_add_u32_e32 v7, 1, v1
	v_cmp_ge_u32_e32 vcc, v6, v4
	s_nop 1
	v_cndmask_b32_e32 v1, v1, v7, vcc
	v_mul_lo_u32 v6, v4, v1
	v_add_u32_e32 v4, v6, v4
	v_cmp_ne_u32_e32 vcc, v5, v4
	v_sub_u32_e32 v7, v4, v6
	v_add_u32_e32 v1, 1, v1
	v_lshlrev_b32_e32 v1, 8, v1
	v_readlane_b32 s6, v253, 10
	v_readlane_b32 s7, v253, 11
	s_waitcnt lgkmcnt(0)
	s_cbranch_vccnz .Lnb_nl_0
	buffer_wbl2 sc1
	buffer_inv sc1
	s_add_u32 s12, s16, 0x6400
	s_addc_u32 s13, s17, 0
	s_mov_b32 s14, 16
	s_waitcnt vmcnt(1)
